# P0 transposes throttle: 4 of 8 waves per workgroup stream weight tiles (half the concurrent HBM streams)
# baseline (speedup 1.0000x reference)
.Lp0_go:
	s_cmp_lt_u32 s91, 4
	s_cbranch_scc1 .Lp0_tw
	s_movk_i32 s99, 0x4000
.Lp0_tw:
	s_lshl_b32 s0, s99, 2
	s_add_i32 s8, s0, s91
	s_mov_b32 s0, 24
	s_ashr_i32 s1, s0, 31
	s_lshl_b32 s10, s98, 2
	s_lshl_b64 s[0:1], s[0:1], 3
	s_add_u32 s0, s92, s0
	s_addc_u32 s1, s93, s1
	s_load_dwordx2 s[6:7], s[0:1], 0x0
	s_cmp_gt_i32 s8, 0xaf7f
	v_mbcnt_lo_u32_b32 v0, -1, 0
	v_mbcnt_hi_u32_b32 v0, -1, v0
	s_cbranch_scc1 .LBB0_898
	s_mul_i32 s0, s91, 0x2100
	s_add_i32 s0, s0, 0
	v_lshlrev_b32_e32 v1, 2, v0
	s_waitcnt lgkmcnt(0)
	s_add_u32 s14, s6, 0x17000000
	v_bfe_u32 v136, v0, 3, 3
	v_and_b32_e32 v2, 28, v1
	s_movk_i32 s1, 0x84
	v_mov_b32_e32 v1, 0x420
	s_addc_u32 s15, s7, 0
	v_mad_u32_u24 v147, v136, s1, v1
	v_mov_b32_e32 v1, 0xc60
	s_add_u32 s9, s6, 0x6e00000
	v_mad_u32_u24 v151, v136, s1, v1
	v_mov_b32_e32 v1, 0x14a0
	s_addc_u32 s11, s7, 0
	v_mad_u32_u24 v153, v136, s1, v1
	v_mov_b32_e32 v1, 0x18c0
	s_add_u32 s17, s6, 0x5a00000
	v_lshl_add_u32 v144, v2, 2, s0
	v_mad_u32_u24 v1, v136, s1, v1
	s_addc_u32 s44, s7, 0
	v_add_u32_e32 v154, v144, v1
	v_lshlrev_b32_e32 v1, 3, v0
	s_add_u32 s45, s6, 0xa00000
	v_and_b32_e32 v140, 56, v1
	s_addc_u32 s46, s7, 0
	v_or_b32_e32 v146, 8, v136
	v_or_b32_e32 v148, 16, v136
	v_or_b32_e32 v150, 24, v136
	v_mul_u32_u24_e32 v1, 0x84, v140
	v_lshlrev_b32_e32 v4, 2, v136
	s_add_u32 s47, s6, 0x4e00000
	v_mad_u32_u24 v145, v136, s1, v144
	v_bfe_u32 v3, v0, 3, 2
	v_add3_u32 v155, s0, v1, v4
	v_lshrrev_b32_e32 v0, 2, v0
	v_lshlrev_b32_e32 v1, 1, v146
	v_lshlrev_b32_e32 v4, 1, v148
	v_lshlrev_b32_e32 v5, 1, v150
	s_addc_u32 s48, s7, 0
	s_lshl_b32 s0, s99, 4
	s_lshl_b32 s1, s91, 2
	v_mov_b32_e32 v139, 0
	s_movk_i32 s2, 0x420
	v_and_b32_e32 v0, 8, v0
	v_and_b32_e32 v1, 24, v1
	v_and_b32_e32 v4, 40, v4
	v_and_b32_e32 v5, 56, v5
	s_add_i32 s1, s1, s0
	s_mov_b32 s5, 0
	v_add3_u32 v149, v147, v144, s2
	v_add3_u32 v152, v151, v144, s2
	v_mov_b32_e32 v141, v139
	v_or_b32_e32 v156, v0, v3
	v_or_b32_e32 v157, v1, v3
	v_or_b32_e32 v158, v4, v3
	v_or_b32_e32 v159, v5, v3
	v_or3_b32 v160, v136, v0, 4
	v_or3_b32 v161, v136, v1, 4
	v_or3_b32 v162, v136, v4, 4
	v_or3_b32 v163, v136, v5, 4
	v_mov_b32_e32 v137, v139
	s_sub_i32 s49, 0, s1
	s_lshl_b32 s50, s98, 4
	s_sub_i32 s51, 0x251fc, s1
	v_lshlrev_b32_e32 v142, 2, v2
	v_mov_b32_e32 v143, v139
	v_mov_b32_e32 v164, 0xffffff40
	s_movk_i32 s52, 0x200
	s_movk_i32 s53, 0xa00
	s_movk_i32 s54, 0xf600
	s_mov_b32 s16, 0x42800000
	v_mov_b32_e32 v165, 0x400
	v_mov_b32_e32 v166, 0xfffffa00
	v_mov_b32_e32 v167, 0xfffffe00
	s_mov_b32 s55, s8
	s_branch .LBB0_18
